# pool_diff (P0) rewritten: 16-deep register rings for new/oldest row loads, counted vmcnt, same f32 arithmetic order
# speedup vs baseline: 1.0241x; 1.0053x over previous
.LBB0_233:
	s_or_b64 exec, exec, s[0:1]
	s_add_i32 s1, 0, 0x23a40
	s_add_i32 s2, 0, 0x23a44
	v_mov_b32_e32 v1, s1
	v_mov_b32_e32 v2, s2
	v_mbcnt_lo_u32_b32 v0, -1, 0
	v_mbcnt_hi_u32_b32 v0, -1, v0
	ds_read_b32 v1, v1
	ds_read_b32 v2, v2
	s_lshl_b32 s0, s90, 3
	s_add_i32 s40, s0, s89
	s_mov_b32 s1, 0
	s_cmpk_gt_i32 s40, 0xfff
	s_waitcnt lgkmcnt(1)
	v_readfirstlane_b32 s38, v1
	s_waitcnt lgkmcnt(0)
	v_readfirstlane_b32 s39, v2
	s_cbranch_scc1 .LBB0_271
	s_lshl_b32 s0, s90, 5
	s_add_i32 s42, s0, s46
	s_bfe_u32 s45, s94, 0x30006
	s_bfe_u32 s0, s89, 0x20001
	s_lshl_b32 s41, s87, 3
	s_lshl_b32 s43, 2, s0
	s_lshl_b32 s2, s45, 9
	s_add_u32 s46, s66, s2
	s_addc_u32 s47, s67, 0
	s_sub_i32 s2, 1, s43
	s_sub_i32 s4, 2, s43
	s_sub_i32 s6, 3, s43
	s_sub_i32 s8, 4, s43
	s_sub_i32 s10, 5, s43
	s_sub_i32 s12, 6, s43
	s_sub_i32 s16, 7, s43
	s_sub_i32 s18, 8, s43
	s_sub_i32 s20, 9, s43
	s_sub_i32 s22, 10, s43
	s_sub_i32 s24, 11, s43
	s_sub_i32 s26, 12, s43
	s_sub_i32 s28, 13, s43
	s_sub_i32 s30, 14, s43
	s_sub_i32 s34, 15, s43
	s_ashr_i32 s3, s2, 31
	s_ashr_i32 s5, s4, 31
	s_ashr_i32 s7, s6, 31
	s_ashr_i32 s9, s8, 31
	s_ashr_i32 s11, s10, 31
	s_ashr_i32 s13, s12, 31
	s_ashr_i32 s17, s16, 31
	s_ashr_i32 s19, s18, 31
	s_ashr_i32 s21, s20, 31
	s_ashr_i32 s23, s22, 31
	s_ashr_i32 s25, s24, 31
	s_ashr_i32 s27, s26, 31
	s_ashr_i32 s29, s28, 31
	s_ashr_i32 s31, s30, 31
	s_ashr_i32 s35, s34, 31
	s_lshl_b32 s36, 0xffffc000, s0
	s_lshl_b32 s0, 0x4000, s0
	s_lshl_b64 s[2:3], s[2:3], 13
	s_lshl_b64 s[4:5], s[4:5], 13
	s_lshl_b64 s[6:7], s[6:7], 13
	s_lshl_b64 s[8:9], s[8:9], 13
	s_lshl_b64 s[10:11], s[10:11], 13
	s_lshl_b64 s[12:13], s[12:13], 13
	s_lshl_b64 s[16:17], s[16:17], 13
	s_lshl_b64 s[18:19], s[18:19], 13
	s_lshl_b64 s[20:21], s[20:21], 13
	s_lshl_b64 s[22:23], s[22:23], 13
	s_lshl_b64 s[24:25], s[24:25], 13
	s_lshl_b64 s[26:27], s[26:27], 13
	s_lshl_b64 s[28:29], s[28:29], 13
	s_lshl_b64 s[30:31], s[30:31], 13
	s_lshl_b64 s[34:35], s[34:35], 13
	s_ashr_i32 s37, s36, 31
	s_xor_b32 s0, s0, 0x3e000
	s_lshl_b32 s45, s45, 10
	v_lshlrev_b32_e32 v2, 2, v0
	s_add_u32 s38, s38, s45
	v_ashrrev_i32_e32 v3, 31, v2
	s_addc_u32 s39, s39, 0
	v_lshl_add_u64 v[0:1], v[2:3], 2, s[38:39]
	v_lshl_add_u64 v[2:3], v[2:3], 1, s[46:47]
	s_mov_b64 s[38:39], 0x4da00000
	v_lshl_add_u64 v[2:3], v[2:3], 0, s[38:39]
	s_movk_i32 s38, 0xe000
	s_mov_b32 s39, -1
	s_mov_b32 s78, s73
	s_mov_b32 s44, 0x3e000
	s_waitcnt vmcnt(14)
	v_lshl_add_u64 v[4:5], v[0:1], 0, s[38:39]
	s_mov_b32 s45, 0x10000
	s_mov_b32 s46, 0x12000
	s_mov_b32 s47, 0x14000
	s_mov_b32 s48, 0x16000
	s_mov_b32 s49, 0x18000
	s_mov_b32 s50, 0x1a000
	s_mov_b32 s51, 0x1c000
	s_mov_b32 s52, 0x1e000
	s_mov_b32 s53, 0x20000
	s_mov_b32 s54, 0x22000
	s_mov_b32 s55, 0x24000
	s_mov_b32 s56, 0x26000
	s_mov_b32 s57, 0x28000
	s_mov_b32 s58, 0x2a000
	s_mov_b32 s59, 0x2c000
	s_mov_b32 s60, 0x2e000
	s_mov_b32 s61, 0x30000
	s_mov_b32 s62, 0x32000
	s_mov_b32 s63, 0x34000
	s_mov_b32 s68, 0x36000
	s_mov_b32 s69, 0x38000
	s_mov_b32 s70, 0x3a000
	s_mov_b32 s71, 0x3c000
	s_waitcnt vmcnt(0)
	s_branch .LBB0_236
.LBB0_236:
	s_lshl_b32 s73, s40, 2
	s_and_b32 s72, s73, 0xfe0
	s_and_b32 s73, s73, 0xffffffe0
	s_add_i32 s77, s43, -1
	s_cmp_eq_u32 s72, 0
	s_cselect_b32 s74, s43, 0
	s_cselect_b32 s42, s73, 0
	s_cselect_b32 s77, 0, s77
	s_ff1_i32_b32 s75, s43
	s_sub_i32 s75, 127, s75
	s_lshl_b32 s75, s75, 23
	s_mov_b32 s99, 0
	s_cmp_lt_u32 s77, 1
	s_cbranch_scc1 .Lpd_pre_issued
	s_sub_i32 s76, s73, 1
	s_lshl_b32 s98, s76, 13
	v_lshl_add_u64 v[178:179], v[0:1], 0, s[98:99]
	global_load_dwordx4 v[180:183], v[178:179], off
	s_cmp_lt_u32 s77, 2
	s_cbranch_scc1 .Lpd_pre_issued
	s_sub_i32 s76, s73, 2
	s_lshl_b32 s98, s76, 13
	v_lshl_add_u64 v[178:179], v[0:1], 0, s[98:99]
	global_load_dwordx4 v[184:187], v[178:179], off
	s_cmp_lt_u32 s77, 3
	s_cbranch_scc1 .Lpd_pre_issued
	s_sub_i32 s76, s73, 3
	s_lshl_b32 s98, s76, 13
	v_lshl_add_u64 v[178:179], v[0:1], 0, s[98:99]
	global_load_dwordx4 v[188:191], v[178:179], off
	s_cmp_lt_u32 s77, 4
	s_cbranch_scc1 .Lpd_pre_issued
	s_sub_i32 s76, s73, 4
	s_lshl_b32 s98, s76, 13
	v_lshl_add_u64 v[178:179], v[0:1], 0, s[98:99]
	global_load_dwordx4 v[192:195], v[178:179], off
	s_cmp_lt_u32 s77, 5
	s_cbranch_scc1 .Lpd_pre_issued
	s_sub_i32 s76, s73, 5
	s_lshl_b32 s98, s76, 13
	v_lshl_add_u64 v[178:179], v[0:1], 0, s[98:99]
	global_load_dwordx4 v[196:199], v[178:179], off
	s_cmp_lt_u32 s77, 6
	s_cbranch_scc1 .Lpd_pre_issued
	s_sub_i32 s76, s73, 6
	s_lshl_b32 s98, s76, 13
	v_lshl_add_u64 v[178:179], v[0:1], 0, s[98:99]
	global_load_dwordx4 v[200:203], v[178:179], off
	s_cmp_lt_u32 s77, 7
	s_cbranch_scc1 .Lpd_pre_issued
	s_sub_i32 s76, s73, 7
	s_lshl_b32 s98, s76, 13
	v_lshl_add_u64 v[178:179], v[0:1], 0, s[98:99]
	global_load_dwordx4 v[204:207], v[178:179], off
	s_cmp_lt_u32 s77, 8
	s_cbranch_scc1 .Lpd_pre_issued
	s_sub_i32 s76, s73, 8
	s_lshl_b32 s98, s76, 13
	v_lshl_add_u64 v[178:179], v[0:1], 0, s[98:99]
	global_load_dwordx4 v[208:211], v[178:179], off
	s_cmp_lt_u32 s77, 9
	s_cbranch_scc1 .Lpd_pre_issued
	s_sub_i32 s76, s73, 9
	s_lshl_b32 s98, s76, 13
	v_lshl_add_u64 v[178:179], v[0:1], 0, s[98:99]
	global_load_dwordx4 v[212:215], v[178:179], off
	s_cmp_lt_u32 s77, 10
	s_cbranch_scc1 .Lpd_pre_issued
	s_sub_i32 s76, s73, 10
	s_lshl_b32 s98, s76, 13
	v_lshl_add_u64 v[178:179], v[0:1], 0, s[98:99]
	global_load_dwordx4 v[216:219], v[178:179], off
	s_cmp_lt_u32 s77, 11
	s_cbranch_scc1 .Lpd_pre_issued
	s_sub_i32 s76, s73, 11
	s_lshl_b32 s98, s76, 13
	v_lshl_add_u64 v[178:179], v[0:1], 0, s[98:99]
	global_load_dwordx4 v[220:223], v[178:179], off
	s_cmp_lt_u32 s77, 12
	s_cbranch_scc1 .Lpd_pre_issued
	s_sub_i32 s76, s73, 12
	s_lshl_b32 s98, s76, 13
	v_lshl_add_u64 v[178:179], v[0:1], 0, s[98:99]
	global_load_dwordx4 v[224:227], v[178:179], off
	s_cmp_lt_u32 s77, 13
	s_cbranch_scc1 .Lpd_pre_issued
	s_sub_i32 s76, s73, 13
	s_lshl_b32 s98, s76, 13
	v_lshl_add_u64 v[178:179], v[0:1], 0, s[98:99]
	global_load_dwordx4 v[228:231], v[178:179], off
	s_cmp_lt_u32 s77, 14
	s_cbranch_scc1 .Lpd_pre_issued
	s_sub_i32 s76, s73, 14
	s_lshl_b32 s98, s76, 13
	v_lshl_add_u64 v[178:179], v[0:1], 0, s[98:99]
	global_load_dwordx4 v[232:235], v[178:179], off
	s_cmp_lt_u32 s77, 15
	s_cbranch_scc1 .Lpd_pre_issued
	s_sub_i32 s76, s73, 15
	s_lshl_b32 s98, s76, 13
	v_lshl_add_u64 v[178:179], v[0:1], 0, s[98:99]
	global_load_dwordx4 v[236:239], v[178:179], off
.Lpd_pre_issued:
	s_add_i32 s76, s73, 0
	s_lshl_b32 s98, s76, 13
	v_lshl_add_u64 v[178:179], v[0:1], 0, s[98:99]
	global_load_dwordx4 v[40:43], v[178:179], off
	s_add_i32 s76, s73, 1
	s_sub_i32 s76, s76, s43
	s_max_i32 s76, s76, s42
	s_lshl_b32 s98, s76, 13
	v_lshl_add_u64 v[178:179], v[0:1], 0, s[98:99]
	global_load_dwordx4 v[104:107], v[178:179], off
	s_add_i32 s76, s73, 1
	s_lshl_b32 s98, s76, 13
	v_lshl_add_u64 v[178:179], v[0:1], 0, s[98:99]
	global_load_dwordx4 v[44:47], v[178:179], off
	s_add_i32 s76, s73, 2
	s_sub_i32 s76, s76, s43
	s_max_i32 s76, s76, s42
	s_lshl_b32 s98, s76, 13
	v_lshl_add_u64 v[178:179], v[0:1], 0, s[98:99]
	global_load_dwordx4 v[108:111], v[178:179], off
	s_add_i32 s76, s73, 2
	s_lshl_b32 s98, s76, 13
	v_lshl_add_u64 v[178:179], v[0:1], 0, s[98:99]
	global_load_dwordx4 v[48:51], v[178:179], off
	s_add_i32 s76, s73, 3
	s_sub_i32 s76, s76, s43
	s_max_i32 s76, s76, s42
	s_lshl_b32 s98, s76, 13
	v_lshl_add_u64 v[178:179], v[0:1], 0, s[98:99]
	global_load_dwordx4 v[112:115], v[178:179], off
	s_add_i32 s76, s73, 3
	s_lshl_b32 s98, s76, 13
	v_lshl_add_u64 v[178:179], v[0:1], 0, s[98:99]
	global_load_dwordx4 v[52:55], v[178:179], off
	s_add_i32 s76, s73, 4
	s_sub_i32 s76, s76, s43
	s_max_i32 s76, s76, s42
	s_lshl_b32 s98, s76, 13
	v_lshl_add_u64 v[178:179], v[0:1], 0, s[98:99]
	global_load_dwordx4 v[116:119], v[178:179], off
	s_add_i32 s76, s73, 4
	s_lshl_b32 s98, s76, 13
	v_lshl_add_u64 v[178:179], v[0:1], 0, s[98:99]
	global_load_dwordx4 v[56:59], v[178:179], off
	s_add_i32 s76, s73, 5
	s_sub_i32 s76, s76, s43
	s_max_i32 s76, s76, s42
	s_lshl_b32 s98, s76, 13
	v_lshl_add_u64 v[178:179], v[0:1], 0, s[98:99]
	global_load_dwordx4 v[120:123], v[178:179], off
	s_add_i32 s76, s73, 5
	s_lshl_b32 s98, s76, 13
	v_lshl_add_u64 v[178:179], v[0:1], 0, s[98:99]
	global_load_dwordx4 v[60:63], v[178:179], off
	s_add_i32 s76, s73, 6
	s_sub_i32 s76, s76, s43
	s_max_i32 s76, s76, s42
	s_lshl_b32 s98, s76, 13
	v_lshl_add_u64 v[178:179], v[0:1], 0, s[98:99]
	global_load_dwordx4 v[124:127], v[178:179], off
	s_add_i32 s76, s73, 6
	s_lshl_b32 s98, s76, 13
	v_lshl_add_u64 v[178:179], v[0:1], 0, s[98:99]
	global_load_dwordx4 v[64:67], v[178:179], off
	s_add_i32 s76, s73, 7
	s_sub_i32 s76, s76, s43
	s_max_i32 s76, s76, s42
	s_lshl_b32 s98, s76, 13
	v_lshl_add_u64 v[178:179], v[0:1], 0, s[98:99]
	global_load_dwordx4 v[128:131], v[178:179], off
	s_add_i32 s76, s73, 7
	s_lshl_b32 s98, s76, 13
	v_lshl_add_u64 v[178:179], v[0:1], 0, s[98:99]
	global_load_dwordx4 v[68:71], v[178:179], off
	s_add_i32 s76, s73, 8
	s_sub_i32 s76, s76, s43
	s_max_i32 s76, s76, s42
	s_lshl_b32 s98, s76, 13
	v_lshl_add_u64 v[178:179], v[0:1], 0, s[98:99]
	global_load_dwordx4 v[132:135], v[178:179], off
	s_add_i32 s76, s73, 8
	s_lshl_b32 s98, s76, 13
	v_lshl_add_u64 v[178:179], v[0:1], 0, s[98:99]
	global_load_dwordx4 v[72:75], v[178:179], off
	s_add_i32 s76, s73, 9
	s_sub_i32 s76, s76, s43
	s_max_i32 s76, s76, s42
	s_lshl_b32 s98, s76, 13
	v_lshl_add_u64 v[178:179], v[0:1], 0, s[98:99]
	global_load_dwordx4 v[136:139], v[178:179], off
	s_add_i32 s76, s73, 9
	s_lshl_b32 s98, s76, 13
	v_lshl_add_u64 v[178:179], v[0:1], 0, s[98:99]
	global_load_dwordx4 v[76:79], v[178:179], off
	s_add_i32 s76, s73, 10
	s_sub_i32 s76, s76, s43
	s_max_i32 s76, s76, s42
	s_lshl_b32 s98, s76, 13
	v_lshl_add_u64 v[178:179], v[0:1], 0, s[98:99]
	global_load_dwordx4 v[140:143], v[178:179], off
	s_add_i32 s76, s73, 10
	s_lshl_b32 s98, s76, 13
	v_lshl_add_u64 v[178:179], v[0:1], 0, s[98:99]
	global_load_dwordx4 v[80:83], v[178:179], off
	s_add_i32 s76, s73, 11
	s_sub_i32 s76, s76, s43
	s_max_i32 s76, s76, s42
	s_lshl_b32 s98, s76, 13
	v_lshl_add_u64 v[178:179], v[0:1], 0, s[98:99]
	global_load_dwordx4 v[144:147], v[178:179], off
	s_add_i32 s76, s73, 11
	s_lshl_b32 s98, s76, 13
	v_lshl_add_u64 v[178:179], v[0:1], 0, s[98:99]
	global_load_dwordx4 v[84:87], v[178:179], off
	s_add_i32 s76, s73, 12
	s_sub_i32 s76, s76, s43
	s_max_i32 s76, s76, s42
	s_lshl_b32 s98, s76, 13
	v_lshl_add_u64 v[178:179], v[0:1], 0, s[98:99]
	global_load_dwordx4 v[148:151], v[178:179], off
	s_add_i32 s76, s73, 12
	s_lshl_b32 s98, s76, 13
	v_lshl_add_u64 v[178:179], v[0:1], 0, s[98:99]
	global_load_dwordx4 v[88:91], v[178:179], off
	s_add_i32 s76, s73, 13
	s_sub_i32 s76, s76, s43
	s_max_i32 s76, s76, s42
	s_lshl_b32 s98, s76, 13
	v_lshl_add_u64 v[178:179], v[0:1], 0, s[98:99]
	global_load_dwordx4 v[152:155], v[178:179], off
	s_add_i32 s76, s73, 13
	s_lshl_b32 s98, s76, 13
	v_lshl_add_u64 v[178:179], v[0:1], 0, s[98:99]
	global_load_dwordx4 v[92:95], v[178:179], off
	s_add_i32 s76, s73, 14
	s_sub_i32 s76, s76, s43
	s_max_i32 s76, s76, s42
	s_lshl_b32 s98, s76, 13
	v_lshl_add_u64 v[178:179], v[0:1], 0, s[98:99]
	global_load_dwordx4 v[156:159], v[178:179], off
	s_add_i32 s76, s73, 14
	s_lshl_b32 s98, s76, 13
	v_lshl_add_u64 v[178:179], v[0:1], 0, s[98:99]
	global_load_dwordx4 v[96:99], v[178:179], off
	s_add_i32 s76, s73, 15
	s_sub_i32 s76, s76, s43
	s_max_i32 s76, s76, s42
	s_lshl_b32 s98, s76, 13
	v_lshl_add_u64 v[178:179], v[0:1], 0, s[98:99]
	global_load_dwordx4 v[160:163], v[178:179], off
	s_add_i32 s76, s73, 15
	s_lshl_b32 s98, s76, 13
	v_lshl_add_u64 v[178:179], v[0:1], 0, s[98:99]
	global_load_dwordx4 v[100:103], v[178:179], off
	s_add_i32 s76, s73, 16
	s_sub_i32 s76, s76, s43
	s_max_i32 s76, s76, s42
	s_lshl_b32 s98, s76, 13
	v_lshl_add_u64 v[178:179], v[0:1], 0, s[98:99]
	global_load_dwordx4 v[164:167], v[178:179], off
	s_waitcnt vmcnt(32)
	v_mov_b32_e32 v168, 0
	v_mov_b32_e32 v169, 0
	v_mov_b32_e32 v170, 0
	v_mov_b32_e32 v171, 0
	s_cmp_lt_u32 s77, 1
	s_cbranch_scc1 .Lpd_pre_summed
	v_pk_add_f32 v[168:169], v[168:169], v[180:181]
	v_pk_add_f32 v[170:171], v[170:171], v[182:183]
	s_cmp_lt_u32 s77, 2
	s_cbranch_scc1 .Lpd_pre_summed
	v_pk_add_f32 v[168:169], v[168:169], v[184:185]
	v_pk_add_f32 v[170:171], v[170:171], v[186:187]
	s_cmp_lt_u32 s77, 3
	s_cbranch_scc1 .Lpd_pre_summed
	v_pk_add_f32 v[168:169], v[168:169], v[188:189]
	v_pk_add_f32 v[170:171], v[170:171], v[190:191]
	s_cmp_lt_u32 s77, 4
	s_cbranch_scc1 .Lpd_pre_summed
	v_pk_add_f32 v[168:169], v[168:169], v[192:193]
	v_pk_add_f32 v[170:171], v[170:171], v[194:195]
	s_cmp_lt_u32 s77, 5
	s_cbranch_scc1 .Lpd_pre_summed
	v_pk_add_f32 v[168:169], v[168:169], v[196:197]
	v_pk_add_f32 v[170:171], v[170:171], v[198:199]
	s_cmp_lt_u32 s77, 6
	s_cbranch_scc1 .Lpd_pre_summed
	v_pk_add_f32 v[168:169], v[168:169], v[200:201]
	v_pk_add_f32 v[170:171], v[170:171], v[202:203]
	s_cmp_lt_u32 s77, 7
	s_cbranch_scc1 .Lpd_pre_summed
	v_pk_add_f32 v[168:169], v[168:169], v[204:205]
	v_pk_add_f32 v[170:171], v[170:171], v[206:207]
	s_cmp_lt_u32 s77, 8
	s_cbranch_scc1 .Lpd_pre_summed
	v_pk_add_f32 v[168:169], v[168:169], v[208:209]
	v_pk_add_f32 v[170:171], v[170:171], v[210:211]
	s_cmp_lt_u32 s77, 9
	s_cbranch_scc1 .Lpd_pre_summed
	v_pk_add_f32 v[168:169], v[168:169], v[212:213]
	v_pk_add_f32 v[170:171], v[170:171], v[214:215]
	s_cmp_lt_u32 s77, 10
	s_cbranch_scc1 .Lpd_pre_summed
	v_pk_add_f32 v[168:169], v[168:169], v[216:217]
	v_pk_add_f32 v[170:171], v[170:171], v[218:219]
	s_cmp_lt_u32 s77, 11
	s_cbranch_scc1 .Lpd_pre_summed
	v_pk_add_f32 v[168:169], v[168:169], v[220:221]
	v_pk_add_f32 v[170:171], v[170:171], v[222:223]
	s_cmp_lt_u32 s77, 12
	s_cbranch_scc1 .Lpd_pre_summed
	v_pk_add_f32 v[168:169], v[168:169], v[224:225]
	v_pk_add_f32 v[170:171], v[170:171], v[226:227]
	s_cmp_lt_u32 s77, 13
	s_cbranch_scc1 .Lpd_pre_summed
	v_pk_add_f32 v[168:169], v[168:169], v[228:229]
	v_pk_add_f32 v[170:171], v[170:171], v[230:231]
	s_cmp_lt_u32 s77, 14
	s_cbranch_scc1 .Lpd_pre_summed
	v_pk_add_f32 v[168:169], v[168:169], v[232:233]
	v_pk_add_f32 v[170:171], v[170:171], v[234:235]
	s_cmp_lt_u32 s77, 15
	s_cbranch_scc1 .Lpd_pre_summed
	v_pk_add_f32 v[168:169], v[168:169], v[236:237]
	v_pk_add_f32 v[170:171], v[170:171], v[238:239]
.Lpd_pre_summed:
	s_waitcnt vmcnt(31)
	v_pk_add_f32 v[168:169], v[168:169], v[40:41]
	v_pk_add_f32 v[170:171], v[170:171], v[42:43]
	s_cmp_lt_u32 1, s74
	s_cselect_b32 s76, 0x3f800000, s75
	v_fma_f32 v172, s76, v168, -v40
	v_fma_f32 v173, s76, v169, -v41
	v_fma_f32 v174, s76, v170, -v42
	v_fma_f32 v175, s76, v171, -v43
	v_cvt_pk_bf16_f32 v176, v172, v173
	v_cvt_pk_bf16_f32 v177, v174, v175
	s_add_i32 s100, s73, 0
	s_lshl_b32 s98, s100, 12
	v_lshl_add_u64 v[178:179], v[2:3], 0, s[98:99]
	global_store_dwordx2 v[178:179], v[176:177], off
	s_add_i32 s76, s73, 16
	s_lshl_b32 s98, s76, 13
	v_lshl_add_u64 v[178:179], v[0:1], 0, s[98:99]
	global_load_dwordx4 v[40:43], v[178:179], off
	s_cmp_lt_u32 1, s74
	s_cbranch_scc1 .Lpd_keep_0
	s_waitcnt vmcnt(32)
	v_sub_f32_e32 v168, v168, v104
	v_sub_f32_e32 v169, v169, v105
	v_sub_f32_e32 v170, v170, v106
	v_sub_f32_e32 v171, v171, v107
.Lpd_keep_0:
	s_add_i32 s76, s73, 17
	s_sub_i32 s76, s76, s43
	s_max_i32 s76, s76, s42
	s_lshl_b32 s98, s76, 13
	v_lshl_add_u64 v[178:179], v[0:1], 0, s[98:99]
	global_load_dwordx4 v[104:107], v[178:179], off
	s_waitcnt vmcnt(32)
	v_pk_add_f32 v[168:169], v[168:169], v[44:45]
	v_pk_add_f32 v[170:171], v[170:171], v[46:47]
	s_cmp_lt_u32 2, s74
	s_cselect_b32 s76, 0x3f000000, s75
	v_fma_f32 v172, s76, v168, -v44
	v_fma_f32 v173, s76, v169, -v45
	v_fma_f32 v174, s76, v170, -v46
	v_fma_f32 v175, s76, v171, -v47
	v_cvt_pk_bf16_f32 v176, v172, v173
	v_cvt_pk_bf16_f32 v177, v174, v175
	s_add_i32 s100, s73, 1
	s_lshl_b32 s98, s100, 12
	v_lshl_add_u64 v[178:179], v[2:3], 0, s[98:99]
	global_store_dwordx2 v[178:179], v[176:177], off
	s_add_i32 s76, s73, 17
	s_lshl_b32 s98, s76, 13
	v_lshl_add_u64 v[178:179], v[0:1], 0, s[98:99]
	global_load_dwordx4 v[44:47], v[178:179], off
	s_cmp_lt_u32 2, s74
	s_cbranch_scc1 .Lpd_keep_1
	s_waitcnt vmcnt(33)
	v_sub_f32_e32 v168, v168, v108
	v_sub_f32_e32 v169, v169, v109
	v_sub_f32_e32 v170, v170, v110
	v_sub_f32_e32 v171, v171, v111
.Lpd_keep_1:
	s_add_i32 s76, s73, 18
	s_sub_i32 s76, s76, s43
	s_max_i32 s76, s76, s42
	s_lshl_b32 s98, s76, 13
	v_lshl_add_u64 v[178:179], v[0:1], 0, s[98:99]
	global_load_dwordx4 v[108:111], v[178:179], off
	s_waitcnt vmcnt(33)
	v_pk_add_f32 v[168:169], v[168:169], v[48:49]
	v_pk_add_f32 v[170:171], v[170:171], v[50:51]
	s_cmp_lt_u32 3, s74
	s_cselect_b32 s76, 0x3eaaaaab, s75
	v_fma_f32 v172, s76, v168, -v48
	v_fma_f32 v173, s76, v169, -v49
	v_fma_f32 v174, s76, v170, -v50
	v_fma_f32 v175, s76, v171, -v51
	v_cvt_pk_bf16_f32 v176, v172, v173
	v_cvt_pk_bf16_f32 v177, v174, v175
	s_add_i32 s100, s73, 2
	s_lshl_b32 s98, s100, 12
	v_lshl_add_u64 v[178:179], v[2:3], 0, s[98:99]
	global_store_dwordx2 v[178:179], v[176:177], off
	s_add_i32 s76, s73, 18
	s_lshl_b32 s98, s76, 13
	v_lshl_add_u64 v[178:179], v[0:1], 0, s[98:99]
	global_load_dwordx4 v[48:51], v[178:179], off
	s_cmp_lt_u32 3, s74
	s_cbranch_scc1 .Lpd_keep_2
	s_waitcnt vmcnt(34)
	v_sub_f32_e32 v168, v168, v112
	v_sub_f32_e32 v169, v169, v113
	v_sub_f32_e32 v170, v170, v114
	v_sub_f32_e32 v171, v171, v115
.Lpd_keep_2:
	s_add_i32 s76, s73, 19
	s_sub_i32 s76, s76, s43
	s_max_i32 s76, s76, s42
	s_lshl_b32 s98, s76, 13
	v_lshl_add_u64 v[178:179], v[0:1], 0, s[98:99]
	global_load_dwordx4 v[112:115], v[178:179], off
	s_waitcnt vmcnt(34)
	v_pk_add_f32 v[168:169], v[168:169], v[52:53]
	v_pk_add_f32 v[170:171], v[170:171], v[54:55]
	s_cmp_lt_u32 4, s74
	s_cselect_b32 s76, 0x3e800000, s75
	v_fma_f32 v172, s76, v168, -v52
	v_fma_f32 v173, s76, v169, -v53
	v_fma_f32 v174, s76, v170, -v54
	v_fma_f32 v175, s76, v171, -v55
	v_cvt_pk_bf16_f32 v176, v172, v173
	v_cvt_pk_bf16_f32 v177, v174, v175
	s_add_i32 s100, s73, 3
	s_lshl_b32 s98, s100, 12
	v_lshl_add_u64 v[178:179], v[2:3], 0, s[98:99]
	global_store_dwordx2 v[178:179], v[176:177], off
	s_add_i32 s76, s73, 19
	s_lshl_b32 s98, s76, 13
	v_lshl_add_u64 v[178:179], v[0:1], 0, s[98:99]
	global_load_dwordx4 v[52:55], v[178:179], off
	s_cmp_lt_u32 4, s74
	s_cbranch_scc1 .Lpd_keep_3
	s_waitcnt vmcnt(35)
	v_sub_f32_e32 v168, v168, v116
	v_sub_f32_e32 v169, v169, v117
	v_sub_f32_e32 v170, v170, v118
	v_sub_f32_e32 v171, v171, v119
.Lpd_keep_3:
	s_add_i32 s76, s73, 20
	s_sub_i32 s76, s76, s43
	s_max_i32 s76, s76, s42
	s_lshl_b32 s98, s76, 13
	v_lshl_add_u64 v[178:179], v[0:1], 0, s[98:99]
	global_load_dwordx4 v[116:119], v[178:179], off
	s_waitcnt vmcnt(35)
	v_pk_add_f32 v[168:169], v[168:169], v[56:57]
	v_pk_add_f32 v[170:171], v[170:171], v[58:59]
	s_cmp_lt_u32 5, s74
	s_cselect_b32 s76, 0x3e4ccccd, s75
	v_fma_f32 v172, s76, v168, -v56
	v_fma_f32 v173, s76, v169, -v57
	v_fma_f32 v174, s76, v170, -v58
	v_fma_f32 v175, s76, v171, -v59
	v_cvt_pk_bf16_f32 v176, v172, v173
	v_cvt_pk_bf16_f32 v177, v174, v175
	s_add_i32 s100, s73, 4
	s_lshl_b32 s98, s100, 12
	v_lshl_add_u64 v[178:179], v[2:3], 0, s[98:99]
	global_store_dwordx2 v[178:179], v[176:177], off
	s_add_i32 s76, s73, 20
	s_lshl_b32 s98, s76, 13
	v_lshl_add_u64 v[178:179], v[0:1], 0, s[98:99]
	global_load_dwordx4 v[56:59], v[178:179], off
	s_cmp_lt_u32 5, s74
	s_cbranch_scc1 .Lpd_keep_4
	s_waitcnt vmcnt(36)
	v_sub_f32_e32 v168, v168, v120
	v_sub_f32_e32 v169, v169, v121
	v_sub_f32_e32 v170, v170, v122
	v_sub_f32_e32 v171, v171, v123
.Lpd_keep_4:
	s_add_i32 s76, s73, 21
	s_sub_i32 s76, s76, s43
	s_max_i32 s76, s76, s42
	s_lshl_b32 s98, s76, 13
	v_lshl_add_u64 v[178:179], v[0:1], 0, s[98:99]
	global_load_dwordx4 v[120:123], v[178:179], off
	s_waitcnt vmcnt(36)
	v_pk_add_f32 v[168:169], v[168:169], v[60:61]
	v_pk_add_f32 v[170:171], v[170:171], v[62:63]
	s_cmp_lt_u32 6, s74
	s_cselect_b32 s76, 0x3e2aaaab, s75
	v_fma_f32 v172, s76, v168, -v60
	v_fma_f32 v173, s76, v169, -v61
	v_fma_f32 v174, s76, v170, -v62
	v_fma_f32 v175, s76, v171, -v63
	v_cvt_pk_bf16_f32 v176, v172, v173
	v_cvt_pk_bf16_f32 v177, v174, v175
	s_add_i32 s100, s73, 5
	s_lshl_b32 s98, s100, 12
	v_lshl_add_u64 v[178:179], v[2:3], 0, s[98:99]
	global_store_dwordx2 v[178:179], v[176:177], off
	s_add_i32 s76, s73, 21
	s_lshl_b32 s98, s76, 13
	v_lshl_add_u64 v[178:179], v[0:1], 0, s[98:99]
	global_load_dwordx4 v[60:63], v[178:179], off
	s_cmp_lt_u32 6, s74
	s_cbranch_scc1 .Lpd_keep_5
	s_waitcnt vmcnt(37)
	v_sub_f32_e32 v168, v168, v124
	v_sub_f32_e32 v169, v169, v125
	v_sub_f32_e32 v170, v170, v126
	v_sub_f32_e32 v171, v171, v127
.Lpd_keep_5:
	s_add_i32 s76, s73, 22
	s_sub_i32 s76, s76, s43
	s_max_i32 s76, s76, s42
	s_lshl_b32 s98, s76, 13
	v_lshl_add_u64 v[178:179], v[0:1], 0, s[98:99]
	global_load_dwordx4 v[124:127], v[178:179], off
	s_waitcnt vmcnt(37)
	v_pk_add_f32 v[168:169], v[168:169], v[64:65]
	v_pk_add_f32 v[170:171], v[170:171], v[66:67]
	s_cmp_lt_u32 7, s74
	s_cselect_b32 s76, 0x3e124925, s75
	v_fma_f32 v172, s76, v168, -v64
	v_fma_f32 v173, s76, v169, -v65
	v_fma_f32 v174, s76, v170, -v66
	v_fma_f32 v175, s76, v171, -v67
	v_cvt_pk_bf16_f32 v176, v172, v173
	v_cvt_pk_bf16_f32 v177, v174, v175
	s_add_i32 s100, s73, 6
	s_lshl_b32 s98, s100, 12
	v_lshl_add_u64 v[178:179], v[2:3], 0, s[98:99]
	global_store_dwordx2 v[178:179], v[176:177], off
	s_add_i32 s76, s73, 22
	s_lshl_b32 s98, s76, 13
	v_lshl_add_u64 v[178:179], v[0:1], 0, s[98:99]
	global_load_dwordx4 v[64:67], v[178:179], off
	s_cmp_lt_u32 7, s74
	s_cbranch_scc1 .Lpd_keep_6
	s_waitcnt vmcnt(38)
	v_sub_f32_e32 v168, v168, v128
	v_sub_f32_e32 v169, v169, v129
	v_sub_f32_e32 v170, v170, v130
	v_sub_f32_e32 v171, v171, v131
.Lpd_keep_6:
	s_add_i32 s76, s73, 23
	s_sub_i32 s76, s76, s43
	s_max_i32 s76, s76, s42
	s_lshl_b32 s98, s76, 13
	v_lshl_add_u64 v[178:179], v[0:1], 0, s[98:99]
	global_load_dwordx4 v[128:131], v[178:179], off
	s_waitcnt vmcnt(38)
	v_pk_add_f32 v[168:169], v[168:169], v[68:69]
	v_pk_add_f32 v[170:171], v[170:171], v[70:71]
	s_cmp_lt_u32 8, s74
	s_cselect_b32 s76, 0x3e000000, s75
	v_fma_f32 v172, s76, v168, -v68
	v_fma_f32 v173, s76, v169, -v69
	v_fma_f32 v174, s76, v170, -v70
	v_fma_f32 v175, s76, v171, -v71
	v_cvt_pk_bf16_f32 v176, v172, v173
	v_cvt_pk_bf16_f32 v177, v174, v175
	s_add_i32 s100, s73, 7
	s_lshl_b32 s98, s100, 12
	v_lshl_add_u64 v[178:179], v[2:3], 0, s[98:99]
	global_store_dwordx2 v[178:179], v[176:177], off
	s_add_i32 s76, s73, 23
	s_lshl_b32 s98, s76, 13
	v_lshl_add_u64 v[178:179], v[0:1], 0, s[98:99]
	global_load_dwordx4 v[68:71], v[178:179], off
	s_cmp_lt_u32 8, s74
	s_cbranch_scc1 .Lpd_keep_7
	s_waitcnt vmcnt(39)
	v_sub_f32_e32 v168, v168, v132
	v_sub_f32_e32 v169, v169, v133
	v_sub_f32_e32 v170, v170, v134
	v_sub_f32_e32 v171, v171, v135
.Lpd_keep_7:
	s_add_i32 s76, s73, 24
	s_sub_i32 s76, s76, s43
	s_max_i32 s76, s76, s42
	s_lshl_b32 s98, s76, 13
	v_lshl_add_u64 v[178:179], v[0:1], 0, s[98:99]
	global_load_dwordx4 v[132:135], v[178:179], off
	s_waitcnt vmcnt(39)
	v_pk_add_f32 v[168:169], v[168:169], v[72:73]
	v_pk_add_f32 v[170:171], v[170:171], v[74:75]
	s_cmp_lt_u32 9, s74
	s_cselect_b32 s76, 0x3de38e39, s75
	v_fma_f32 v172, s76, v168, -v72
	v_fma_f32 v173, s76, v169, -v73
	v_fma_f32 v174, s76, v170, -v74
	v_fma_f32 v175, s76, v171, -v75
	v_cvt_pk_bf16_f32 v176, v172, v173
	v_cvt_pk_bf16_f32 v177, v174, v175
	s_add_i32 s100, s73, 8
	s_lshl_b32 s98, s100, 12
	v_lshl_add_u64 v[178:179], v[2:3], 0, s[98:99]
	global_store_dwordx2 v[178:179], v[176:177], off
	s_add_i32 s76, s73, 24
	s_lshl_b32 s98, s76, 13
	v_lshl_add_u64 v[178:179], v[0:1], 0, s[98:99]
	global_load_dwordx4 v[72:75], v[178:179], off
	s_cmp_lt_u32 9, s74
	s_cbranch_scc1 .Lpd_keep_8
	s_waitcnt vmcnt(40)
	v_sub_f32_e32 v168, v168, v136
	v_sub_f32_e32 v169, v169, v137
	v_sub_f32_e32 v170, v170, v138
	v_sub_f32_e32 v171, v171, v139
.Lpd_keep_8:
	s_add_i32 s76, s73, 25
	s_sub_i32 s76, s76, s43
	s_max_i32 s76, s76, s42
	s_lshl_b32 s98, s76, 13
	v_lshl_add_u64 v[178:179], v[0:1], 0, s[98:99]
	global_load_dwordx4 v[136:139], v[178:179], off
	s_waitcnt vmcnt(40)
	v_pk_add_f32 v[168:169], v[168:169], v[76:77]
	v_pk_add_f32 v[170:171], v[170:171], v[78:79]
	s_cmp_lt_u32 10, s74
	s_cselect_b32 s76, 0x3dcccccd, s75
	v_fma_f32 v172, s76, v168, -v76
	v_fma_f32 v173, s76, v169, -v77
	v_fma_f32 v174, s76, v170, -v78
	v_fma_f32 v175, s76, v171, -v79
	v_cvt_pk_bf16_f32 v176, v172, v173
	v_cvt_pk_bf16_f32 v177, v174, v175
	s_add_i32 s100, s73, 9
	s_lshl_b32 s98, s100, 12
	v_lshl_add_u64 v[178:179], v[2:3], 0, s[98:99]
	global_store_dwordx2 v[178:179], v[176:177], off
	s_add_i32 s76, s73, 25
	s_lshl_b32 s98, s76, 13
	v_lshl_add_u64 v[178:179], v[0:1], 0, s[98:99]
	global_load_dwordx4 v[76:79], v[178:179], off
	s_cmp_lt_u32 10, s74
	s_cbranch_scc1 .Lpd_keep_9
	s_waitcnt vmcnt(41)
	v_sub_f32_e32 v168, v168, v140
	v_sub_f32_e32 v169, v169, v141
	v_sub_f32_e32 v170, v170, v142
	v_sub_f32_e32 v171, v171, v143
.Lpd_keep_9:
	s_add_i32 s76, s73, 26
	s_sub_i32 s76, s76, s43
	s_max_i32 s76, s76, s42
	s_lshl_b32 s98, s76, 13
	v_lshl_add_u64 v[178:179], v[0:1], 0, s[98:99]
	global_load_dwordx4 v[140:143], v[178:179], off
	s_waitcnt vmcnt(41)
	v_pk_add_f32 v[168:169], v[168:169], v[80:81]
	v_pk_add_f32 v[170:171], v[170:171], v[82:83]
	s_cmp_lt_u32 11, s74
	s_cselect_b32 s76, 0x3dba2e8c, s75
	v_fma_f32 v172, s76, v168, -v80
	v_fma_f32 v173, s76, v169, -v81
	v_fma_f32 v174, s76, v170, -v82
	v_fma_f32 v175, s76, v171, -v83
	v_cvt_pk_bf16_f32 v176, v172, v173
	v_cvt_pk_bf16_f32 v177, v174, v175
	s_add_i32 s100, s73, 10
	s_lshl_b32 s98, s100, 12
	v_lshl_add_u64 v[178:179], v[2:3], 0, s[98:99]
	global_store_dwordx2 v[178:179], v[176:177], off
	s_add_i32 s76, s73, 26
	s_lshl_b32 s98, s76, 13
	v_lshl_add_u64 v[178:179], v[0:1], 0, s[98:99]
	global_load_dwordx4 v[80:83], v[178:179], off
	s_cmp_lt_u32 11, s74
	s_cbranch_scc1 .Lpd_keep_10
	s_waitcnt vmcnt(42)
	v_sub_f32_e32 v168, v168, v144
	v_sub_f32_e32 v169, v169, v145
	v_sub_f32_e32 v170, v170, v146
	v_sub_f32_e32 v171, v171, v147
.Lpd_keep_10:
	s_add_i32 s76, s73, 27
	s_sub_i32 s76, s76, s43
	s_max_i32 s76, s76, s42
	s_lshl_b32 s98, s76, 13
	v_lshl_add_u64 v[178:179], v[0:1], 0, s[98:99]
	global_load_dwordx4 v[144:147], v[178:179], off
	s_waitcnt vmcnt(42)
	v_pk_add_f32 v[168:169], v[168:169], v[84:85]
	v_pk_add_f32 v[170:171], v[170:171], v[86:87]
	s_cmp_lt_u32 12, s74
	s_cselect_b32 s76, 0x3daaaaab, s75
	v_fma_f32 v172, s76, v168, -v84
	v_fma_f32 v173, s76, v169, -v85
	v_fma_f32 v174, s76, v170, -v86
	v_fma_f32 v175, s76, v171, -v87
	v_cvt_pk_bf16_f32 v176, v172, v173
	v_cvt_pk_bf16_f32 v177, v174, v175
	s_add_i32 s100, s73, 11
	s_lshl_b32 s98, s100, 12
	v_lshl_add_u64 v[178:179], v[2:3], 0, s[98:99]
	global_store_dwordx2 v[178:179], v[176:177], off
	s_add_i32 s76, s73, 27
	s_lshl_b32 s98, s76, 13
	v_lshl_add_u64 v[178:179], v[0:1], 0, s[98:99]
	global_load_dwordx4 v[84:87], v[178:179], off
	s_cmp_lt_u32 12, s74
	s_cbranch_scc1 .Lpd_keep_11
	s_waitcnt vmcnt(43)
	v_sub_f32_e32 v168, v168, v148
	v_sub_f32_e32 v169, v169, v149
	v_sub_f32_e32 v170, v170, v150
	v_sub_f32_e32 v171, v171, v151
.Lpd_keep_11:
	s_add_i32 s76, s73, 28
	s_sub_i32 s76, s76, s43
	s_max_i32 s76, s76, s42
	s_lshl_b32 s98, s76, 13
	v_lshl_add_u64 v[178:179], v[0:1], 0, s[98:99]
	global_load_dwordx4 v[148:151], v[178:179], off
	s_waitcnt vmcnt(43)
	v_pk_add_f32 v[168:169], v[168:169], v[88:89]
	v_pk_add_f32 v[170:171], v[170:171], v[90:91]
	s_cmp_lt_u32 13, s74
	s_cselect_b32 s76, 0x3d9d89d9, s75
	v_fma_f32 v172, s76, v168, -v88
	v_fma_f32 v173, s76, v169, -v89
	v_fma_f32 v174, s76, v170, -v90
	v_fma_f32 v175, s76, v171, -v91
	v_cvt_pk_bf16_f32 v176, v172, v173
	v_cvt_pk_bf16_f32 v177, v174, v175
	s_add_i32 s100, s73, 12
	s_lshl_b32 s98, s100, 12
	v_lshl_add_u64 v[178:179], v[2:3], 0, s[98:99]
	global_store_dwordx2 v[178:179], v[176:177], off
	s_add_i32 s76, s73, 28
	s_lshl_b32 s98, s76, 13
	v_lshl_add_u64 v[178:179], v[0:1], 0, s[98:99]
	global_load_dwordx4 v[88:91], v[178:179], off
	s_cmp_lt_u32 13, s74
	s_cbranch_scc1 .Lpd_keep_12
	s_waitcnt vmcnt(44)
	v_sub_f32_e32 v168, v168, v152
	v_sub_f32_e32 v169, v169, v153
	v_sub_f32_e32 v170, v170, v154
	v_sub_f32_e32 v171, v171, v155
.Lpd_keep_12:
	s_add_i32 s76, s73, 29
	s_sub_i32 s76, s76, s43
	s_max_i32 s76, s76, s42
	s_lshl_b32 s98, s76, 13
	v_lshl_add_u64 v[178:179], v[0:1], 0, s[98:99]
	global_load_dwordx4 v[152:155], v[178:179], off
	s_waitcnt vmcnt(44)
	v_pk_add_f32 v[168:169], v[168:169], v[92:93]
	v_pk_add_f32 v[170:171], v[170:171], v[94:95]
	s_cmp_lt_u32 14, s74
	s_cselect_b32 s76, 0x3d924925, s75
	v_fma_f32 v172, s76, v168, -v92
	v_fma_f32 v173, s76, v169, -v93
	v_fma_f32 v174, s76, v170, -v94
	v_fma_f32 v175, s76, v171, -v95
	v_cvt_pk_bf16_f32 v176, v172, v173
	v_cvt_pk_bf16_f32 v177, v174, v175
	s_add_i32 s100, s73, 13
	s_lshl_b32 s98, s100, 12
	v_lshl_add_u64 v[178:179], v[2:3], 0, s[98:99]
	global_store_dwordx2 v[178:179], v[176:177], off
	s_add_i32 s76, s73, 29
	s_lshl_b32 s98, s76, 13
	v_lshl_add_u64 v[178:179], v[0:1], 0, s[98:99]
	global_load_dwordx4 v[92:95], v[178:179], off
	s_cmp_lt_u32 14, s74
	s_cbranch_scc1 .Lpd_keep_13
	s_waitcnt vmcnt(45)
	v_sub_f32_e32 v168, v168, v156
	v_sub_f32_e32 v169, v169, v157
	v_sub_f32_e32 v170, v170, v158
	v_sub_f32_e32 v171, v171, v159
.Lpd_keep_13:
	s_add_i32 s76, s73, 30
	s_sub_i32 s76, s76, s43
	s_max_i32 s76, s76, s42
	s_lshl_b32 s98, s76, 13
	v_lshl_add_u64 v[178:179], v[0:1], 0, s[98:99]
	global_load_dwordx4 v[156:159], v[178:179], off
	s_waitcnt vmcnt(45)
	v_pk_add_f32 v[168:169], v[168:169], v[96:97]
	v_pk_add_f32 v[170:171], v[170:171], v[98:99]
	s_cmp_lt_u32 15, s74
	s_cselect_b32 s76, 0x3d888889, s75
	v_fma_f32 v172, s76, v168, -v96
	v_fma_f32 v173, s76, v169, -v97
	v_fma_f32 v174, s76, v170, -v98
	v_fma_f32 v175, s76, v171, -v99
	v_cvt_pk_bf16_f32 v176, v172, v173
	v_cvt_pk_bf16_f32 v177, v174, v175
	s_add_i32 s100, s73, 14
	s_lshl_b32 s98, s100, 12
	v_lshl_add_u64 v[178:179], v[2:3], 0, s[98:99]
	global_store_dwordx2 v[178:179], v[176:177], off
	s_add_i32 s76, s73, 30
	s_lshl_b32 s98, s76, 13
	v_lshl_add_u64 v[178:179], v[0:1], 0, s[98:99]
	global_load_dwordx4 v[96:99], v[178:179], off
	s_cmp_lt_u32 15, s74
	s_cbranch_scc1 .Lpd_keep_14
	s_waitcnt vmcnt(46)
	v_sub_f32_e32 v168, v168, v160
	v_sub_f32_e32 v169, v169, v161
	v_sub_f32_e32 v170, v170, v162
	v_sub_f32_e32 v171, v171, v163
.Lpd_keep_14:
	s_add_i32 s76, s73, 31
	s_sub_i32 s76, s76, s43
	s_max_i32 s76, s76, s42
	s_lshl_b32 s98, s76, 13
	v_lshl_add_u64 v[178:179], v[0:1], 0, s[98:99]
	global_load_dwordx4 v[160:163], v[178:179], off
	s_waitcnt vmcnt(46)
	v_pk_add_f32 v[168:169], v[168:169], v[100:101]
	v_pk_add_f32 v[170:171], v[170:171], v[102:103]
	v_fma_f32 v172, s75, v168, -v100
	v_fma_f32 v173, s75, v169, -v101
	v_fma_f32 v174, s75, v170, -v102
	v_fma_f32 v175, s75, v171, -v103
	v_cvt_pk_bf16_f32 v176, v172, v173
	v_cvt_pk_bf16_f32 v177, v174, v175
	s_add_i32 s100, s73, 15
	s_lshl_b32 s98, s100, 12
	v_lshl_add_u64 v[178:179], v[2:3], 0, s[98:99]
	global_store_dwordx2 v[178:179], v[176:177], off
	s_add_i32 s76, s73, 31
	s_lshl_b32 s98, s76, 13
	v_lshl_add_u64 v[178:179], v[0:1], 0, s[98:99]
	global_load_dwordx4 v[100:103], v[178:179], off
	s_waitcnt vmcnt(47)
	v_sub_f32_e32 v168, v168, v164
	v_sub_f32_e32 v169, v169, v165
	v_sub_f32_e32 v170, v170, v166
	v_sub_f32_e32 v171, v171, v167
	s_waitcnt vmcnt(45)
	v_pk_add_f32 v[168:169], v[168:169], v[40:41]
	v_pk_add_f32 v[170:171], v[170:171], v[42:43]
	v_fma_f32 v172, s75, v168, -v40
	v_fma_f32 v173, s75, v169, -v41
	v_fma_f32 v174, s75, v170, -v42
	v_fma_f32 v175, s75, v171, -v43
	v_cvt_pk_bf16_f32 v176, v172, v173
	v_cvt_pk_bf16_f32 v177, v174, v175
	s_add_i32 s100, s73, 16
	s_lshl_b32 s98, s100, 12
	v_lshl_add_u64 v[178:179], v[2:3], 0, s[98:99]
	global_store_dwordx2 v[178:179], v[176:177], off
	s_waitcnt vmcnt(45)
	v_sub_f32_e32 v168, v168, v104
	v_sub_f32_e32 v169, v169, v105
	v_sub_f32_e32 v170, v170, v106
	v_sub_f32_e32 v171, v171, v107
	s_waitcnt vmcnt(43)
	v_pk_add_f32 v[168:169], v[168:169], v[44:45]
	v_pk_add_f32 v[170:171], v[170:171], v[46:47]
	v_fma_f32 v172, s75, v168, -v44
	v_fma_f32 v173, s75, v169, -v45
	v_fma_f32 v174, s75, v170, -v46
	v_fma_f32 v175, s75, v171, -v47
	v_cvt_pk_bf16_f32 v176, v172, v173
	v_cvt_pk_bf16_f32 v177, v174, v175
	s_add_i32 s100, s73, 17
	s_lshl_b32 s98, s100, 12
	v_lshl_add_u64 v[178:179], v[2:3], 0, s[98:99]
	global_store_dwordx2 v[178:179], v[176:177], off
	s_waitcnt vmcnt(43)
	v_sub_f32_e32 v168, v168, v108
	v_sub_f32_e32 v169, v169, v109
	v_sub_f32_e32 v170, v170, v110
	v_sub_f32_e32 v171, v171, v111
	s_waitcnt vmcnt(41)
	v_pk_add_f32 v[168:169], v[168:169], v[48:49]
	v_pk_add_f32 v[170:171], v[170:171], v[50:51]
	v_fma_f32 v172, s75, v168, -v48
	v_fma_f32 v173, s75, v169, -v49
	v_fma_f32 v174, s75, v170, -v50
	v_fma_f32 v175, s75, v171, -v51
	v_cvt_pk_bf16_f32 v176, v172, v173
	v_cvt_pk_bf16_f32 v177, v174, v175
	s_add_i32 s100, s73, 18
	s_lshl_b32 s98, s100, 12
	v_lshl_add_u64 v[178:179], v[2:3], 0, s[98:99]
	global_store_dwordx2 v[178:179], v[176:177], off
	s_waitcnt vmcnt(41)
	v_sub_f32_e32 v168, v168, v112
	v_sub_f32_e32 v169, v169, v113
	v_sub_f32_e32 v170, v170, v114
	v_sub_f32_e32 v171, v171, v115
	s_waitcnt vmcnt(39)
	v_pk_add_f32 v[168:169], v[168:169], v[52:53]
	v_pk_add_f32 v[170:171], v[170:171], v[54:55]
	v_fma_f32 v172, s75, v168, -v52
	v_fma_f32 v173, s75, v169, -v53
	v_fma_f32 v174, s75, v170, -v54
	v_fma_f32 v175, s75, v171, -v55
	v_cvt_pk_bf16_f32 v176, v172, v173
	v_cvt_pk_bf16_f32 v177, v174, v175
	s_add_i32 s100, s73, 19
	s_lshl_b32 s98, s100, 12
	v_lshl_add_u64 v[178:179], v[2:3], 0, s[98:99]
	global_store_dwordx2 v[178:179], v[176:177], off
	s_waitcnt vmcnt(39)
	v_sub_f32_e32 v168, v168, v116
	v_sub_f32_e32 v169, v169, v117
	v_sub_f32_e32 v170, v170, v118
	v_sub_f32_e32 v171, v171, v119
	s_waitcnt vmcnt(37)
	v_pk_add_f32 v[168:169], v[168:169], v[56:57]
	v_pk_add_f32 v[170:171], v[170:171], v[58:59]
	v_fma_f32 v172, s75, v168, -v56
	v_fma_f32 v173, s75, v169, -v57
	v_fma_f32 v174, s75, v170, -v58
	v_fma_f32 v175, s75, v171, -v59
	v_cvt_pk_bf16_f32 v176, v172, v173
	v_cvt_pk_bf16_f32 v177, v174, v175
	s_add_i32 s100, s73, 20
	s_lshl_b32 s98, s100, 12
	v_lshl_add_u64 v[178:179], v[2:3], 0, s[98:99]
	global_store_dwordx2 v[178:179], v[176:177], off
	s_waitcnt vmcnt(37)
	v_sub_f32_e32 v168, v168, v120
	v_sub_f32_e32 v169, v169, v121
	v_sub_f32_e32 v170, v170, v122
	v_sub_f32_e32 v171, v171, v123
	s_waitcnt vmcnt(35)
	v_pk_add_f32 v[168:169], v[168:169], v[60:61]
	v_pk_add_f32 v[170:171], v[170:171], v[62:63]
	v_fma_f32 v172, s75, v168, -v60
	v_fma_f32 v173, s75, v169, -v61
	v_fma_f32 v174, s75, v170, -v62
	v_fma_f32 v175, s75, v171, -v63
	v_cvt_pk_bf16_f32 v176, v172, v173
	v_cvt_pk_bf16_f32 v177, v174, v175
	s_add_i32 s100, s73, 21
	s_lshl_b32 s98, s100, 12
	v_lshl_add_u64 v[178:179], v[2:3], 0, s[98:99]
	global_store_dwordx2 v[178:179], v[176:177], off
	s_waitcnt vmcnt(35)
	v_sub_f32_e32 v168, v168, v124
	v_sub_f32_e32 v169, v169, v125
	v_sub_f32_e32 v170, v170, v126
	v_sub_f32_e32 v171, v171, v127
	s_waitcnt vmcnt(33)
	v_pk_add_f32 v[168:169], v[168:169], v[64:65]
	v_pk_add_f32 v[170:171], v[170:171], v[66:67]
	v_fma_f32 v172, s75, v168, -v64
	v_fma_f32 v173, s75, v169, -v65
	v_fma_f32 v174, s75, v170, -v66
	v_fma_f32 v175, s75, v171, -v67
	v_cvt_pk_bf16_f32 v176, v172, v173
	v_cvt_pk_bf16_f32 v177, v174, v175
	s_add_i32 s100, s73, 22
	s_lshl_b32 s98, s100, 12
	v_lshl_add_u64 v[178:179], v[2:3], 0, s[98:99]
	global_store_dwordx2 v[178:179], v[176:177], off
	s_waitcnt vmcnt(33)
	v_sub_f32_e32 v168, v168, v128
	v_sub_f32_e32 v169, v169, v129
	v_sub_f32_e32 v170, v170, v130
	v_sub_f32_e32 v171, v171, v131
	s_waitcnt vmcnt(31)
	v_pk_add_f32 v[168:169], v[168:169], v[68:69]
	v_pk_add_f32 v[170:171], v[170:171], v[70:71]
	v_fma_f32 v172, s75, v168, -v68
	v_fma_f32 v173, s75, v169, -v69
	v_fma_f32 v174, s75, v170, -v70
	v_fma_f32 v175, s75, v171, -v71
	v_cvt_pk_bf16_f32 v176, v172, v173
	v_cvt_pk_bf16_f32 v177, v174, v175
	s_add_i32 s100, s73, 23
	s_lshl_b32 s98, s100, 12
	v_lshl_add_u64 v[178:179], v[2:3], 0, s[98:99]
	global_store_dwordx2 v[178:179], v[176:177], off
	s_waitcnt vmcnt(31)
	v_sub_f32_e32 v168, v168, v132
	v_sub_f32_e32 v169, v169, v133
	v_sub_f32_e32 v170, v170, v134
	v_sub_f32_e32 v171, v171, v135
	s_waitcnt vmcnt(29)
	v_pk_add_f32 v[168:169], v[168:169], v[72:73]
	v_pk_add_f32 v[170:171], v[170:171], v[74:75]
	v_fma_f32 v172, s75, v168, -v72
	v_fma_f32 v173, s75, v169, -v73
	v_fma_f32 v174, s75, v170, -v74
	v_fma_f32 v175, s75, v171, -v75
	v_cvt_pk_bf16_f32 v176, v172, v173
	v_cvt_pk_bf16_f32 v177, v174, v175
	s_add_i32 s100, s73, 24
	s_lshl_b32 s98, s100, 12
	v_lshl_add_u64 v[178:179], v[2:3], 0, s[98:99]
	global_store_dwordx2 v[178:179], v[176:177], off
	s_waitcnt vmcnt(29)
	v_sub_f32_e32 v168, v168, v136
	v_sub_f32_e32 v169, v169, v137
	v_sub_f32_e32 v170, v170, v138
	v_sub_f32_e32 v171, v171, v139
	s_waitcnt vmcnt(27)
	v_pk_add_f32 v[168:169], v[168:169], v[76:77]
	v_pk_add_f32 v[170:171], v[170:171], v[78:79]
	v_fma_f32 v172, s75, v168, -v76
	v_fma_f32 v173, s75, v169, -v77
	v_fma_f32 v174, s75, v170, -v78
	v_fma_f32 v175, s75, v171, -v79
	v_cvt_pk_bf16_f32 v176, v172, v173
	v_cvt_pk_bf16_f32 v177, v174, v175
	s_add_i32 s100, s73, 25
	s_lshl_b32 s98, s100, 12
	v_lshl_add_u64 v[178:179], v[2:3], 0, s[98:99]
	global_store_dwordx2 v[178:179], v[176:177], off
	s_waitcnt vmcnt(27)
	v_sub_f32_e32 v168, v168, v140
	v_sub_f32_e32 v169, v169, v141
	v_sub_f32_e32 v170, v170, v142
	v_sub_f32_e32 v171, v171, v143
	s_waitcnt vmcnt(25)
	v_pk_add_f32 v[168:169], v[168:169], v[80:81]
	v_pk_add_f32 v[170:171], v[170:171], v[82:83]
	v_fma_f32 v172, s75, v168, -v80
	v_fma_f32 v173, s75, v169, -v81
	v_fma_f32 v174, s75, v170, -v82
	v_fma_f32 v175, s75, v171, -v83
	v_cvt_pk_bf16_f32 v176, v172, v173
	v_cvt_pk_bf16_f32 v177, v174, v175
	s_add_i32 s100, s73, 26
	s_lshl_b32 s98, s100, 12
	v_lshl_add_u64 v[178:179], v[2:3], 0, s[98:99]
	global_store_dwordx2 v[178:179], v[176:177], off
	s_waitcnt vmcnt(25)
	v_sub_f32_e32 v168, v168, v144
	v_sub_f32_e32 v169, v169, v145
	v_sub_f32_e32 v170, v170, v146
	v_sub_f32_e32 v171, v171, v147
	s_waitcnt vmcnt(23)
	v_pk_add_f32 v[168:169], v[168:169], v[84:85]
	v_pk_add_f32 v[170:171], v[170:171], v[86:87]
	v_fma_f32 v172, s75, v168, -v84
	v_fma_f32 v173, s75, v169, -v85
	v_fma_f32 v174, s75, v170, -v86
	v_fma_f32 v175, s75, v171, -v87
	v_cvt_pk_bf16_f32 v176, v172, v173
	v_cvt_pk_bf16_f32 v177, v174, v175
	s_add_i32 s100, s73, 27
	s_lshl_b32 s98, s100, 12
	v_lshl_add_u64 v[178:179], v[2:3], 0, s[98:99]
	global_store_dwordx2 v[178:179], v[176:177], off
	s_waitcnt vmcnt(23)
	v_sub_f32_e32 v168, v168, v148
	v_sub_f32_e32 v169, v169, v149
	v_sub_f32_e32 v170, v170, v150
	v_sub_f32_e32 v171, v171, v151
	s_waitcnt vmcnt(21)
	v_pk_add_f32 v[168:169], v[168:169], v[88:89]
	v_pk_add_f32 v[170:171], v[170:171], v[90:91]
	v_fma_f32 v172, s75, v168, -v88
	v_fma_f32 v173, s75, v169, -v89
	v_fma_f32 v174, s75, v170, -v90
	v_fma_f32 v175, s75, v171, -v91
	v_cvt_pk_bf16_f32 v176, v172, v173
	v_cvt_pk_bf16_f32 v177, v174, v175
	s_add_i32 s100, s73, 28
	s_lshl_b32 s98, s100, 12
	v_lshl_add_u64 v[178:179], v[2:3], 0, s[98:99]
	global_store_dwordx2 v[178:179], v[176:177], off
	s_waitcnt vmcnt(21)
	v_sub_f32_e32 v168, v168, v152
	v_sub_f32_e32 v169, v169, v153
	v_sub_f32_e32 v170, v170, v154
	v_sub_f32_e32 v171, v171, v155
	s_waitcnt vmcnt(19)
	v_pk_add_f32 v[168:169], v[168:169], v[92:93]
	v_pk_add_f32 v[170:171], v[170:171], v[94:95]
	v_fma_f32 v172, s75, v168, -v92
	v_fma_f32 v173, s75, v169, -v93
	v_fma_f32 v174, s75, v170, -v94
	v_fma_f32 v175, s75, v171, -v95
	v_cvt_pk_bf16_f32 v176, v172, v173
	v_cvt_pk_bf16_f32 v177, v174, v175
	s_add_i32 s100, s73, 29
	s_lshl_b32 s98, s100, 12
	v_lshl_add_u64 v[178:179], v[2:3], 0, s[98:99]
	global_store_dwordx2 v[178:179], v[176:177], off
	s_waitcnt vmcnt(19)
	v_sub_f32_e32 v168, v168, v156
	v_sub_f32_e32 v169, v169, v157
	v_sub_f32_e32 v170, v170, v158
	v_sub_f32_e32 v171, v171, v159
	s_waitcnt vmcnt(17)
	v_pk_add_f32 v[168:169], v[168:169], v[96:97]
	v_pk_add_f32 v[170:171], v[170:171], v[98:99]
	v_fma_f32 v172, s75, v168, -v96
	v_fma_f32 v173, s75, v169, -v97
	v_fma_f32 v174, s75, v170, -v98
	v_fma_f32 v175, s75, v171, -v99
	v_cvt_pk_bf16_f32 v176, v172, v173
	v_cvt_pk_bf16_f32 v177, v174, v175
	s_add_i32 s100, s73, 30
	s_lshl_b32 s98, s100, 12
	v_lshl_add_u64 v[178:179], v[2:3], 0, s[98:99]
	global_store_dwordx2 v[178:179], v[176:177], off
	s_waitcnt vmcnt(17)
	v_sub_f32_e32 v168, v168, v160
	v_sub_f32_e32 v169, v169, v161
	v_sub_f32_e32 v170, v170, v162
	v_sub_f32_e32 v171, v171, v163
	s_waitcnt vmcnt(15)
	v_pk_add_f32 v[168:169], v[168:169], v[100:101]
	v_pk_add_f32 v[170:171], v[170:171], v[102:103]
	v_fma_f32 v172, s75, v168, -v100
	v_fma_f32 v173, s75, v169, -v101
	v_fma_f32 v174, s75, v170, -v102
	v_fma_f32 v175, s75, v171, -v103
	v_cvt_pk_bf16_f32 v176, v172, v173
	v_cvt_pk_bf16_f32 v177, v174, v175
	s_add_i32 s100, s73, 31
	s_lshl_b32 s98, s100, 12
	v_lshl_add_u64 v[178:179], v[2:3], 0, s[98:99]
	global_store_dwordx2 v[178:179], v[176:177], off
	s_add_i32 s40, s40, s41
	s_cmpk_lt_i32 s40, 0x1000
	s_cbranch_scc1 .LBB0_236
